# mixer A key/value loop: prefetch distance 2 (three rotating fragment register sets, unrolled x3, no copies), on top of the combine-phase changes
# baseline (speedup 1.0000x reference)
.LBB0_804:
	s_and_b64 vcc, exec, s[0:1]
	s_cbranch_vccz .LBB0_433
	s_bfe_u32 s8, s68, 0x20009
	s_lshl_b32 s0, s8, 4
	v_mov_b32_e32 v2, s0
	s_ashr_i32 s0, s68, 11
	s_lshl_b32 s6, s0, 2
	s_or_b32 s15, s6, s8
	s_and_b32 s11, s68, 0x1ff
	s_lshl_b32 s6, s15, 13
	s_lshl_b32 s1, s11, 4
	s_ashr_i32 s7, s6, 31
	global_load_dwordx4 v[54:57], v2, s[20:21]
	s_lshl_b64 s[60:61], s[6:7], 6
	s_lshl_b32 s6, s15, 6
	v_or_b32_e32 v2, s1, v149
	s_ashr_i32 s7, s6, 31
	s_add_i32 s11, s11, -8
	s_waitcnt vmcnt(23)
	v_mad_i64_i32 v[4:5], s[64:65], s0, v186, v[168:169]
	v_mul_u32_u24_e32 v2, 0xf00, v2
	s_lshl_b32 s18, s8, 8
	s_lshl_b64 s[62:63], s[6:7], 14
	s_ashr_i32 s6, s11, 1
	v_lshl_add_u64 v[4:5], v[4:5], 0, v[2:3]
	s_or_b32 s10, s18, 64
	s_or_b32 s28, s18, 0x80
	s_or_b32 s30, s18, 0xc0
	v_lshl_add_u64 v[6:7], v[4:5], 0, s[18:19]
	s_mov_b32 s11, s19
	s_mov_b32 s29, s19
	s_mov_b32 s31, s19
	s_max_i32 s7, s6, 0
	v_lshl_add_u64 v[8:9], v[4:5], 0, s[10:11]
	global_load_dwordx4 v[70:73], v[6:7], off nt
	global_load_dwordx4 v[74:77], v[8:9], off nt
	v_lshl_add_u64 v[6:7], v[4:5], 0, s[28:29]
	v_lshl_add_u64 v[4:5], v[4:5], 0, s[30:31]
	v_lshl_add_u64 v[172:173], v[156:157], 0, s[60:61]
	v_lshl_or_b32 v2, s7, 11, v160
	global_load_dwordx4 v[78:81], v[6:7], off nt
	global_load_dwordx4 v[82:85], v[4:5], off nt
	v_lshl_add_u64 v[174:175], v[170:171], 0, s[62:63]
	v_lshl_add_u64 v[4:5], v[172:173], 0, v[2:3]
	s_lshl_b32 s10, s7, 12
	global_load_dwordx4 v[130:133], v[4:5], off
	global_load_dwordx4 v[126:129], v[4:5], off offset:1024
	v_lshl_add_u64 v[4:5], v[174:175], 0, s[10:11]
	global_load_dwordx4 v[114:117], v[4:5], off
	global_load_dwordx4 v[102:105], v[4:5], off offset:1024
	global_load_dwordx4 v[98:101], v[4:5], off offset:2048
	global_load_dwordx4 v[86:89], v[4:5], off offset:3072
	s_mulk_i32 s8, 0x1410
	s_add_i32 s8, s8, 0
	v_lshl_add_u32 v2, s6, 5, v183
	s_addk_i32 s8, 0x280
	v_subrev_u32_e32 v2, s1, v2
	v_mov_b32_e32 v4, v3
	v_mov_b32_e32 v5, v3
	v_lshl_add_u32 v190, v2, 2, s8
	s_mov_b32 s8, 0x3fb8aa3b
	v_mov_b32_e32 v2, v3
	v_mov_b64_e32 v[8:9], v[4:5]
	s_waitcnt vmcnt(31)
	v_mov_b64_e32 v[12:13], v[4:5]
	v_mov_b64_e32 v[16:17], v[4:5]
	s_waitcnt vmcnt(29)
	v_mov_b64_e32 v[20:21], v[4:5]
	s_waitcnt lgkmcnt(0)
	v_mov_b64_e32 v[24:25], v[4:5]
	s_waitcnt vmcnt(27)
	v_mov_b64_e32 v[28:29], v[4:5]
	v_mov_b64_e32 v[32:33], v[4:5]
	s_waitcnt vmcnt(25)
	v_mov_b64_e32 v[36:37], v[4:5]
	v_mov_b64_e32 v[40:41], v[4:5]
	s_waitcnt vmcnt(23)
	v_mov_b64_e32 v[44:45], v[4:5]
	v_mov_b64_e32 v[48:49], v[4:5]
	s_waitcnt vmcnt(21)
	v_mov_b64_e32 v[52:53], v[4:5]
	s_waitcnt vmcnt(19)
	v_mov_b64_e32 v[60:61], v[4:5]
	v_mov_b64_e32 v[64:65], v[4:5]
	s_waitcnt vmcnt(17)
	v_mov_b64_e32 v[68:69], v[4:5]
	s_mov_b32 s7, 1
	v_mov_b32_e32 v187, v163
	v_mov_b32_e32 v188, v163
	v_mov_b32_e32 v189, v163
	v_mov_b64_e32 v[6:7], v[2:3]
	v_mov_b64_e32 v[10:11], v[2:3]
	v_mov_b64_e32 v[14:15], v[2:3]
	v_mov_b64_e32 v[18:19], v[2:3]
	v_mov_b64_e32 v[22:23], v[2:3]
	v_mov_b64_e32 v[26:27], v[2:3]
	v_mov_b64_e32 v[30:31], v[2:3]
	v_mov_b64_e32 v[34:35], v[2:3]
	v_mov_b64_e32 v[38:39], v[2:3]
	v_mov_b64_e32 v[42:43], v[2:3]
	v_mov_b64_e32 v[46:47], v[2:3]
	v_mov_b64_e32 v[50:51], v[2:3]
	v_mov_b64_e32 v[58:59], v[2:3]
	v_mov_b64_e32 v[62:63], v[2:3]
	v_mov_b64_e32 v[66:67], v[2:3]
	s_waitcnt vmcnt(10)
	v_pk_mul_f32 v[176:177], v[54:55], s[8:9] op_sel_hi:[1,0]
	v_pk_mul_f32 v[178:179], v[56:57], s[8:9] op_sel_hi:[1,0]
	v_mov_b64_e32 v[56:57], v[4:5]
	v_mov_b64_e32 v[54:55], v[2:3]
	v_mov_b32_e32 v4, v163
	s_min_u32 s8, s7, 8
	s_add_i32 s8, s8, s6
	v_med3_i32 v5, s8, 0, v184
	v_lshl_or_b32 v2, v5, 11, v160
	v_lshl_add_u64 v[94:95], v[172:173], 0, v[2:3]
	v_lshlrev_b32_e32 v2, 12, v5
	v_lshl_add_u64 v[122:123], v[174:175], 0, v[2:3]
	global_load_dwordx4 v[90:93], v[94:95], off
	s_nop 0
	global_load_dwordx4 v[94:97], v[94:95], off offset:1024
	s_nop 0
	global_load_dwordx4 v[106:109], v[122:123], off
	global_load_dwordx4 v[110:113], v[122:123], off offset:1024
	global_load_dwordx4 v[118:121], v[122:123], off offset:2048
	s_nop 0
	global_load_dwordx4 v[122:125], v[122:123], off offset:3072
.Lpf2a_body_0:
	s_add_i32 s8, s7, 1
	s_cmp_gt_u32 s8, 8
	s_cbranch_scc1 .Lpf2a_nopf_0
	s_add_i32 s8, s8, s6
	v_med3_i32 v5, s8, 0, v184
	v_lshl_or_b32 v2, v5, 11, v160
	v_lshl_add_u64 v[218:219], v[172:173], 0, v[2:3]
	v_lshlrev_b32_e32 v2, 12, v5
	v_lshl_add_u64 v[234:235], v[174:175], 0, v[2:3]
	global_load_dwordx4 v[214:217], v[218:219], off
	s_nop 0
	global_load_dwordx4 v[218:221], v[218:219], off offset:1024
	s_nop 0
	global_load_dwordx4 v[222:225], v[234:235], off
	global_load_dwordx4 v[226:229], v[234:235], off offset:1024
	global_load_dwordx4 v[230:233], v[234:235], off offset:2048
	s_nop 0
	global_load_dwordx4 v[234:237], v[234:235], off offset:3072
.Lpf2a_nopf_0:
	s_add_i32 s8, s6, s7
	s_add_i32 s8, s8, -1
	s_cmpk_gt_u32 s8, 0xff
	s_cbranch_scc1 .Lpf2a_816_0
	ds_read2_b32 v[134:135], v190 offset1:1
	ds_read2_b32 v[136:137], v190 offset0:2 offset1:3
	ds_read2_b32 v[192:193], v190 offset0:16 offset1:17
	ds_read2_b32 v[194:195], v190 offset0:18 offset1:19
	s_waitcnt vmcnt(17) lgkmcnt(2)
	v_mfma_f32_16x16x32_fp8_fp8 v[134:137], v[130:131], v[70:71], v[134:137]
	v_mfma_f32_16x16x32_fp8_fp8 v[138:141], v[132:133], v[72:73], v[134:137]
	s_waitcnt vmcnt(16) lgkmcnt(0)
	v_mfma_f32_16x16x32_fp8_fp8 v[134:137], v[126:127], v[70:71], v[192:195]
	v_mfma_f32_16x16x32_fp8_fp8 v[134:137], v[128:129], v[72:73], v[134:137]
	s_nop 4
	v_max_f32_e32 v2, v139, v139
	v_max_f32_e32 v5, v138, v138
	v_max_f32_e32 v2, v5, v2
	v_max_f32_e32 v5, v141, v141
	v_max_f32_e32 v191, v140, v140
	v_max_f32_e32 v5, v191, v5
	v_max_f32_e32 v191, v137, v137
	v_max_f32_e32 v192, v136, v136
	v_max_f32_e32 v191, v192, v191
	v_max3_f32 v191, v134, v135, v191
	v_max3_f32 v2, v2, v5, v191
	v_mov_b32_e32 v5, v2
	s_nop 1
	v_permlane16_swap_b32_e32 v2, v5
	v_max_f32_e32 v5, v5, v5
	v_max_f32_e32 v2, v2, v2
	v_max_f32_e32 v2, v2, v5
	v_mov_b32_e32 v5, v2
	s_nop 1
	v_permlane32_swap_b32_e32 v2, v5
	v_max_f32_e32 v5, v5, v5
	v_max_f32_e32 v2, v2, v2
	v_max_f32_e32 v2, v2, v5
	v_cmp_gt_f32_e32 vcc, v2, v176
	s_cbranch_vccz .Lpf2a_809_0
	v_max_f32_e32 v2, v2, v2
	v_max_f32_e32 v5, v176, v176
	v_max_f32_e32 v5, v5, v2
	v_sub_f32_e32 v2, v176, v5
	v_exp_f32_e32 v2, v2
	v_mov_b32_e32 v176, v5
	v_mul_f32_e32 v4, v4, v2
	v_pk_mul_f32 v[68:69], v[68:69], v[2:3] op_sel_hi:[1,0]
	v_pk_mul_f32 v[66:67], v[66:67], v[2:3] op_sel_hi:[1,0]
	v_pk_mul_f32 v[64:65], v[64:65], v[2:3] op_sel_hi:[1,0]
	v_pk_mul_f32 v[62:63], v[62:63], v[2:3] op_sel_hi:[1,0]
	v_pk_mul_f32 v[60:61], v[60:61], v[2:3] op_sel_hi:[1,0]
	v_pk_mul_f32 v[58:59], v[58:59], v[2:3] op_sel_hi:[1,0]
	v_pk_mul_f32 v[56:57], v[56:57], v[2:3] op_sel_hi:[1,0]
	v_pk_mul_f32 v[54:55], v[54:55], v[2:3] op_sel_hi:[1,0]
.Lpf2a_809_0:
	v_sub_f32_e32 v134, v134, v176
	v_exp_f32_e32 v193, v134
	v_sub_f32_e32 v134, v135, v176
	v_sub_f32_e32 v2, v138, v176
	v_sub_f32_e32 v138, v140, v176
	v_exp_f32_e32 v194, v134
	v_sub_f32_e32 v134, v136, v176
	v_sub_f32_e32 v5, v139, v176
	v_exp_f32_e32 v191, v138
	v_sub_f32_e32 v138, v141, v176
	v_exp_f32_e32 v195, v134
	v_sub_f32_e32 v134, v137, v176
	v_exp_f32_e32 v2, v2
	v_exp_f32_e32 v5, v5
	v_exp_f32_e32 v192, v138
	v_exp_f32_e32 v196, v134
	v_cvt_pk_bf16_f32 v136, v193, v194
	v_cvt_pk_bf16_f32 v134, v2, v5
	v_cvt_pk_bf16_f32 v135, v191, v192
	v_cvt_pk_bf16_f32 v137, v195, v196
	s_waitcnt vmcnt(15)
	s_nop 0
	v_mfma_f32_16x16x32_bf16 v[66:69], v[114:117], v[134:137], v[66:69]
	s_waitcnt vmcnt(14)
	v_mfma_f32_16x16x32_bf16 v[62:65], v[102:105], v[134:137], v[62:65]
	s_waitcnt vmcnt(13)
	v_mfma_f32_16x16x32_bf16 v[58:61], v[98:101], v[134:137], v[58:61]
	s_waitcnt vmcnt(12)
	v_mfma_f32_16x16x32_bf16 v[54:57], v[86:89], v[134:137], v[54:57]
	v_add_u32_e32 v134, 0x504, v190
	v_add_u32_e32 v136, 0x50c, v190
	ds_read2_b32 v[134:135], v134 offset1:1
	ds_read2_b32 v[136:137], v136 offset1:1
	v_add_u32_e32 v138, 0x544, v190
	ds_read2_b32 v[198:199], v138 offset1:1
	v_add_u32_e32 v138, 0x54c, v190
	ds_read2_b32 v[200:201], v138 offset1:1
	s_waitcnt lgkmcnt(2)
	v_mfma_f32_16x16x32_fp8_fp8 v[134:137], v[130:131], v[74:75], v[134:137]
	v_mfma_f32_16x16x32_fp8_fp8 v[138:141], v[132:133], v[76:77], v[134:137]
	s_waitcnt lgkmcnt(0)
	v_mfma_f32_16x16x32_fp8_fp8 v[134:137], v[126:127], v[74:75], v[198:201]
	v_mfma_f32_16x16x32_fp8_fp8 v[134:137], v[128:129], v[76:77], v[134:137]
	s_nop 4
	v_max_f32_e32 v197, v139, v139
	v_max_f32_e32 v198, v138, v138
	v_max_f32_e32 v197, v198, v197
	v_max_f32_e32 v198, v141, v141
	v_max_f32_e32 v199, v140, v140
	v_max_f32_e32 v198, v199, v198
	v_max_f32_e32 v199, v137, v137
	v_max_f32_e32 v200, v136, v136
	v_max_f32_e32 v199, v200, v199
	v_max3_f32 v199, v134, v135, v199
	v_max3_f32 v197, v197, v198, v199
	v_mov_b32_e32 v198, v197
	s_nop 1
	v_permlane16_swap_b32_e32 v197, v198
	v_max_f32_e32 v198, v198, v198
	v_max_f32_e32 v197, v197, v197
	v_max_f32_e32 v197, v197, v198
	v_mov_b32_e32 v198, v197
	s_nop 1
	v_permlane32_swap_b32_e32 v197, v198
	v_max_f32_e32 v198, v198, v198
	v_max_f32_e32 v197, v197, v197
	v_max_f32_e32 v197, v197, v198
	v_cmp_gt_f32_e32 vcc, v197, v177
	s_cbranch_vccz .Lpf2a_811_0
	v_max_f32_e32 v197, v197, v197
	v_max_f32_e32 v198, v177, v177
	v_max_f32_e32 v197, v198, v197
	v_sub_f32_e32 v177, v177, v197
	v_exp_f32_e32 v198, v177
	v_mov_b32_e32 v177, v197
	v_mul_f32_e32 v189, v189, v198
	v_pk_mul_f32 v[52:53], v[52:53], v[198:199] op_sel_hi:[1,0]
	v_pk_mul_f32 v[50:51], v[50:51], v[198:199] op_sel_hi:[1,0]
	v_pk_mul_f32 v[48:49], v[48:49], v[198:199] op_sel_hi:[1,0]
	v_pk_mul_f32 v[46:47], v[46:47], v[198:199] op_sel_hi:[1,0]
	v_pk_mul_f32 v[44:45], v[44:45], v[198:199] op_sel_hi:[1,0]
	v_pk_mul_f32 v[42:43], v[42:43], v[198:199] op_sel_hi:[1,0]
	v_pk_mul_f32 v[40:41], v[40:41], v[198:199] op_sel_hi:[1,0]
	v_pk_mul_f32 v[38:39], v[38:39], v[198:199] op_sel_hi:[1,0]

.Lpf2a_816_0:
	s_add_i32 s7, s7, 1
	s_cmp_lg_u32 s7, 10
	v_add_u32_e32 v190, 0x80, v190
	s_cbranch_scc0 .LBB0_432
	s_cmp_gt_u32 s7, 8
	s_cbranch_scc1 .Lpf2a_w0_0
	s_waitcnt vmcnt(6)
	s_branch .Lpf2a_body_1

.Lpf2a_body_1:
	s_add_i32 s8, s7, 1
	s_cmp_gt_u32 s8, 8
	s_cbranch_scc1 .Lpf2a_nopf_1
	s_add_i32 s8, s8, s6
	v_med3_i32 v5, s8, 0, v184
	v_lshl_or_b32 v2, v5, 11, v160
	v_lshl_add_u64 v[126:127], v[172:173], 0, v[2:3]
	v_lshlrev_b32_e32 v2, 12, v5
	v_lshl_add_u64 v[86:87], v[174:175], 0, v[2:3]
	global_load_dwordx4 v[130:133], v[126:127], off
	s_nop 0
	global_load_dwordx4 v[126:129], v[126:127], off offset:1024
	s_nop 0
	global_load_dwordx4 v[114:117], v[86:87], off
	global_load_dwordx4 v[102:105], v[86:87], off offset:1024
	global_load_dwordx4 v[98:101], v[86:87], off offset:2048
	s_nop 0
	global_load_dwordx4 v[86:89], v[86:87], off offset:3072
.Lpf2a_nopf_1:
	s_add_i32 s8, s6, s7
	s_add_i32 s8, s8, -1
	s_cmpk_gt_u32 s8, 0xff
	s_cbranch_scc1 .Lpf2a_816_1
	ds_read2_b32 v[134:135], v190 offset1:1
	ds_read2_b32 v[136:137], v190 offset0:2 offset1:3
	ds_read2_b32 v[192:193], v190 offset0:16 offset1:17
	ds_read2_b32 v[194:195], v190 offset0:18 offset1:19
	s_waitcnt vmcnt(17) lgkmcnt(2)
	v_mfma_f32_16x16x32_fp8_fp8 v[134:137], v[90:91], v[70:71], v[134:137]
	v_mfma_f32_16x16x32_fp8_fp8 v[138:141], v[92:93], v[72:73], v[134:137]
	s_waitcnt vmcnt(16) lgkmcnt(0)
	v_mfma_f32_16x16x32_fp8_fp8 v[134:137], v[94:95], v[70:71], v[192:195]
	v_mfma_f32_16x16x32_fp8_fp8 v[134:137], v[96:97], v[72:73], v[134:137]
	s_nop 4
	v_max_f32_e32 v2, v139, v139
	v_max_f32_e32 v5, v138, v138
	v_max_f32_e32 v2, v5, v2
	v_max_f32_e32 v5, v141, v141
	v_max_f32_e32 v191, v140, v140
	v_max_f32_e32 v5, v191, v5
	v_max_f32_e32 v191, v137, v137
	v_max_f32_e32 v192, v136, v136
	v_max_f32_e32 v191, v192, v191
	v_max3_f32 v191, v134, v135, v191
	v_max3_f32 v2, v2, v5, v191
	v_mov_b32_e32 v5, v2
	s_nop 1
	v_permlane16_swap_b32_e32 v2, v5
	v_max_f32_e32 v5, v5, v5
	v_max_f32_e32 v2, v2, v2
	v_max_f32_e32 v2, v2, v5
	v_mov_b32_e32 v5, v2
	s_nop 1
	v_permlane32_swap_b32_e32 v2, v5
	v_max_f32_e32 v5, v5, v5
	v_max_f32_e32 v2, v2, v2
	v_max_f32_e32 v2, v2, v5
	v_cmp_gt_f32_e32 vcc, v2, v176
	s_cbranch_vccz .Lpf2a_809_1
	v_max_f32_e32 v2, v2, v2
	v_max_f32_e32 v5, v176, v176
	v_max_f32_e32 v5, v5, v2
	v_sub_f32_e32 v2, v176, v5
	v_exp_f32_e32 v2, v2
	v_mov_b32_e32 v176, v5
	v_mul_f32_e32 v4, v4, v2
	v_pk_mul_f32 v[68:69], v[68:69], v[2:3] op_sel_hi:[1,0]
	v_pk_mul_f32 v[66:67], v[66:67], v[2:3] op_sel_hi:[1,0]
	v_pk_mul_f32 v[64:65], v[64:65], v[2:3] op_sel_hi:[1,0]
	v_pk_mul_f32 v[62:63], v[62:63], v[2:3] op_sel_hi:[1,0]
	v_pk_mul_f32 v[60:61], v[60:61], v[2:3] op_sel_hi:[1,0]
	v_pk_mul_f32 v[58:59], v[58:59], v[2:3] op_sel_hi:[1,0]
	v_pk_mul_f32 v[56:57], v[56:57], v[2:3] op_sel_hi:[1,0]
	v_pk_mul_f32 v[54:55], v[54:55], v[2:3] op_sel_hi:[1,0]
.Lpf2a_809_1:
	v_sub_f32_e32 v134, v134, v176
	v_exp_f32_e32 v193, v134
	v_sub_f32_e32 v134, v135, v176
	v_sub_f32_e32 v2, v138, v176
	v_sub_f32_e32 v138, v140, v176
	v_exp_f32_e32 v194, v134
	v_sub_f32_e32 v134, v136, v176
	v_sub_f32_e32 v5, v139, v176
	v_exp_f32_e32 v191, v138
	v_sub_f32_e32 v138, v141, v176
	v_exp_f32_e32 v195, v134
	v_sub_f32_e32 v134, v137, v176
	v_exp_f32_e32 v2, v2
	v_exp_f32_e32 v5, v5
	v_exp_f32_e32 v192, v138
	v_exp_f32_e32 v196, v134
	v_cvt_pk_bf16_f32 v136, v193, v194
	v_cvt_pk_bf16_f32 v134, v2, v5
	v_cvt_pk_bf16_f32 v135, v191, v192
	v_cvt_pk_bf16_f32 v137, v195, v196
	s_waitcnt vmcnt(15)
	s_nop 0
	v_mfma_f32_16x16x32_bf16 v[66:69], v[106:109], v[134:137], v[66:69]
	s_waitcnt vmcnt(14)
	v_mfma_f32_16x16x32_bf16 v[62:65], v[110:113], v[134:137], v[62:65]
	s_waitcnt vmcnt(13)
	v_mfma_f32_16x16x32_bf16 v[58:61], v[118:121], v[134:137], v[58:61]
	s_waitcnt vmcnt(12)
	v_mfma_f32_16x16x32_bf16 v[54:57], v[122:125], v[134:137], v[54:57]
	v_add_u32_e32 v134, 0x504, v190
	v_add_u32_e32 v136, 0x50c, v190
	ds_read2_b32 v[134:135], v134 offset1:1
	ds_read2_b32 v[136:137], v136 offset1:1
	v_add_u32_e32 v138, 0x544, v190
	ds_read2_b32 v[198:199], v138 offset1:1
	v_add_u32_e32 v138, 0x54c, v190
	ds_read2_b32 v[200:201], v138 offset1:1
	s_waitcnt lgkmcnt(2)
	v_mfma_f32_16x16x32_fp8_fp8 v[134:137], v[90:91], v[74:75], v[134:137]
	v_mfma_f32_16x16x32_fp8_fp8 v[138:141], v[92:93], v[76:77], v[134:137]
	s_waitcnt lgkmcnt(0)
	v_mfma_f32_16x16x32_fp8_fp8 v[134:137], v[94:95], v[74:75], v[198:201]
	v_mfma_f32_16x16x32_fp8_fp8 v[134:137], v[96:97], v[76:77], v[134:137]
	s_nop 4
	v_max_f32_e32 v197, v139, v139
	v_max_f32_e32 v198, v138, v138
	v_max_f32_e32 v197, v198, v197
	v_max_f32_e32 v198, v141, v141
	v_max_f32_e32 v199, v140, v140
	v_max_f32_e32 v198, v199, v198
	v_max_f32_e32 v199, v137, v137
	v_max_f32_e32 v200, v136, v136
	v_max_f32_e32 v199, v200, v199
	v_max3_f32 v199, v134, v135, v199
	v_max3_f32 v197, v197, v198, v199
	v_mov_b32_e32 v198, v197
	s_nop 1
	v_permlane16_swap_b32_e32 v197, v198
	v_max_f32_e32 v198, v198, v198
	v_max_f32_e32 v197, v197, v197
	v_max_f32_e32 v197, v197, v198
	v_mov_b32_e32 v198, v197
	s_nop 1
	v_permlane32_swap_b32_e32 v197, v198
	v_max_f32_e32 v198, v198, v198
	v_max_f32_e32 v197, v197, v197
	v_max_f32_e32 v197, v197, v198
	v_cmp_gt_f32_e32 vcc, v197, v177
	s_cbranch_vccz .Lpf2a_811_1
	v_max_f32_e32 v197, v197, v197
	v_max_f32_e32 v198, v177, v177
	v_max_f32_e32 v197, v198, v197
	v_sub_f32_e32 v177, v177, v197
	v_exp_f32_e32 v198, v177
	v_mov_b32_e32 v177, v197
	v_mul_f32_e32 v189, v189, v198
	v_pk_mul_f32 v[52:53], v[52:53], v[198:199] op_sel_hi:[1,0]
	v_pk_mul_f32 v[50:51], v[50:51], v[198:199] op_sel_hi:[1,0]
	v_pk_mul_f32 v[48:49], v[48:49], v[198:199] op_sel_hi:[1,0]
	v_pk_mul_f32 v[46:47], v[46:47], v[198:199] op_sel_hi:[1,0]
	v_pk_mul_f32 v[44:45], v[44:45], v[198:199] op_sel_hi:[1,0]
	v_pk_mul_f32 v[42:43], v[42:43], v[198:199] op_sel_hi:[1,0]
	v_pk_mul_f32 v[40:41], v[40:41], v[198:199] op_sel_hi:[1,0]
	v_pk_mul_f32 v[38:39], v[38:39], v[198:199] op_sel_hi:[1,0]
.Lpf2a_811_1:
	v_sub_f32_e32 v138, v138, v177
	v_sub_f32_e32 v134, v134, v177
	v_exp_f32_e32 v197, v138
	v_sub_f32_e32 v138, v139, v177
	v_exp_f32_e32 v201, v134
	v_sub_f32_e32 v134, v135, v177
	v_exp_f32_e32 v198, v138
	v_sub_f32_e32 v138, v140, v177
	v_exp_f32_e32 v202, v134
	v_sub_f32_e32 v134, v136, v177
	v_exp_f32_e32 v199, v138
	v_sub_f32_e32 v138, v141, v177
	v_exp_f32_e32 v203, v134
	v_sub_f32_e32 v134, v137, v177
	v_exp_f32_e32 v200, v138
	v_exp_f32_e32 v204, v134
	v_cvt_pk_bf16_f32 v134, v197, v198
	v_cvt_pk_bf16_f32 v136, v201, v202
	v_cvt_pk_bf16_f32 v135, v199, v200
	v_cvt_pk_bf16_f32 v137, v203, v204
	s_nop 1
	v_mfma_f32_16x16x32_bf16 v[50:53], v[106:109], v[134:137], v[50:53]
	v_mfma_f32_16x16x32_bf16 v[46:49], v[110:113], v[134:137], v[46:49]
	v_mfma_f32_16x16x32_bf16 v[42:45], v[118:121], v[134:137], v[42:45]
	v_mfma_f32_16x16x32_bf16 v[38:41], v[122:125], v[134:137], v[38:41]
	v_add_u32_e32 v134, 0xa08, v190
	v_add_u32_e32 v136, 0xa10, v190
	ds_read2_b32 v[134:135], v134 offset1:1
	ds_read2_b32 v[136:137], v136 offset1:1
	v_add_u32_e32 v138, 0xa48, v190
	ds_read2_b32 v[206:207], v138 offset1:1
	v_add_u32_e32 v138, 0xa50, v190
	ds_read2_b32 v[208:209], v138 offset1:1
	s_waitcnt lgkmcnt(2)
	v_mfma_f32_16x16x32_fp8_fp8 v[134:137], v[90:91], v[78:79], v[134:137]
	v_mfma_f32_16x16x32_fp8_fp8 v[138:141], v[92:93], v[80:81], v[134:137]
	s_waitcnt lgkmcnt(0)
	v_mfma_f32_16x16x32_fp8_fp8 v[134:137], v[94:95], v[78:79], v[206:209]
	v_mfma_f32_16x16x32_fp8_fp8 v[134:137], v[96:97], v[80:81], v[134:137]
	s_nop 4
	v_max_f32_e32 v205, v139, v139
	v_max_f32_e32 v206, v138, v138
	v_max_f32_e32 v205, v206, v205
	v_max_f32_e32 v206, v141, v141
	v_max_f32_e32 v207, v140, v140
	v_max_f32_e32 v206, v207, v206
	v_max_f32_e32 v207, v137, v137
	v_max_f32_e32 v208, v136, v136
	v_max_f32_e32 v207, v208, v207
	v_max3_f32 v207, v134, v135, v207
	v_max3_f32 v205, v205, v206, v207
	v_mov_b32_e32 v206, v205
	s_nop 1
	v_permlane16_swap_b32_e32 v205, v206
	v_max_f32_e32 v206, v206, v206
	v_max_f32_e32 v205, v205, v205
	v_max_f32_e32 v205, v205, v206
	v_mov_b32_e32 v206, v205
	s_nop 1
	v_permlane32_swap_b32_e32 v205, v206
	v_max_f32_e32 v206, v206, v206
	v_max_f32_e32 v205, v205, v205
	v_max_f32_e32 v205, v205, v206
	v_cmp_gt_f32_e32 vcc, v205, v178
	s_cbranch_vccz .Lpf2a_813_1
	v_max_f32_e32 v205, v205, v205
	v_max_f32_e32 v206, v178, v178
	v_max_f32_e32 v205, v206, v205
	v_sub_f32_e32 v178, v178, v205
	v_exp_f32_e32 v178, v178
	s_nop 0
	v_mul_f32_e32 v188, v188, v178
	v_pk_mul_f32 v[36:37], v[36:37], v[178:179] op_sel_hi:[1,0]
	v_pk_mul_f32 v[34:35], v[34:35], v[178:179] op_sel_hi:[1,0]
	v_pk_mul_f32 v[32:33], v[32:33], v[178:179] op_sel_hi:[1,0]
	v_pk_mul_f32 v[30:31], v[30:31], v[178:179] op_sel_hi:[1,0]
	v_pk_mul_f32 v[28:29], v[28:29], v[178:179] op_sel_hi:[1,0]
	v_pk_mul_f32 v[26:27], v[26:27], v[178:179] op_sel_hi:[1,0]
	v_pk_mul_f32 v[24:25], v[24:25], v[178:179] op_sel_hi:[1,0]
	v_pk_mul_f32 v[22:23], v[22:23], v[178:179] op_sel_hi:[1,0]
	v_mov_b32_e32 v178, v205
.Lpf2a_813_1:
	v_sub_f32_e32 v138, v138, v178
	v_sub_f32_e32 v139, v139, v178
	v_sub_f32_e32 v140, v140, v178
	v_sub_f32_e32 v141, v141, v178
	v_sub_f32_e32 v134, v134, v178
	v_sub_f32_e32 v135, v135, v178
	v_sub_f32_e32 v136, v136, v178
	v_sub_f32_e32 v137, v137, v178
	v_exp_f32_e32 v138, v138
	v_exp_f32_e32 v139, v139
	v_exp_f32_e32 v140, v140
	v_exp_f32_e32 v141, v141
	v_exp_f32_e32 v134, v134
	v_exp_f32_e32 v135, v135
	v_exp_f32_e32 v136, v136
	v_exp_f32_e32 v137, v137
	v_cvt_pk_bf16_f32 v206, v138, v139
	v_cvt_pk_bf16_f32 v207, v140, v141
	v_cvt_pk_bf16_f32 v208, v134, v135
	v_cvt_pk_bf16_f32 v209, v136, v137
	s_nop 1
	v_mfma_f32_16x16x32_bf16 v[34:37], v[106:109], v[206:209], v[34:37]
	v_mfma_f32_16x16x32_bf16 v[30:33], v[110:113], v[206:209], v[30:33]
	v_mfma_f32_16x16x32_bf16 v[26:29], v[118:121], v[206:209], v[26:29]
	v_mfma_f32_16x16x32_bf16 v[22:25], v[122:125], v[206:209], v[22:25]
	v_add_u32_e32 v205, 0xf0c, v190
	v_add_u32_e32 v208, 0xf14, v190
	ds_read2_b32 v[206:207], v205 offset1:1
	ds_read2_b32 v[208:209], v208 offset1:1
	v_add_u32_e32 v205, 0xf4c, v190
	v_add_u32_e32 v212, 0xf54, v190
	ds_read2_b32 v[210:211], v205 offset1:1
	ds_read2_b32 v[212:213], v212 offset1:1
	s_waitcnt lgkmcnt(2)
	v_mfma_f32_16x16x32_fp8_fp8 v[206:209], v[90:91], v[82:83], v[206:209]
	s_waitcnt lgkmcnt(0)
	v_mfma_f32_16x16x32_fp8_fp8 v[210:213], v[94:95], v[82:83], v[210:213]
	v_mfma_f32_16x16x32_fp8_fp8 v[90:93], v[92:93], v[84:85], v[206:209]
	v_mfma_f32_16x16x32_fp8_fp8 v[94:97], v[96:97], v[84:85], v[210:213]
	s_nop 6
	v_max_f32_e32 v205, v91, v91
	v_max_f32_e32 v206, v90, v90
	v_max_f32_e32 v207, v93, v93
	v_max_f32_e32 v205, v206, v205
	v_max_f32_e32 v206, v92, v92
	v_max_f32_e32 v206, v206, v207
	v_max_f32_e32 v207, v97, v97
	v_max_f32_e32 v208, v96, v96
	v_max_f32_e32 v207, v208, v207
	v_max3_f32 v207, v94, v95, v207
	v_max3_f32 v205, v205, v206, v207
	v_mov_b32_e32 v206, v205
	s_nop 1
	v_permlane16_swap_b32_e32 v205, v206
	v_max_f32_e32 v206, v206, v206
	v_max_f32_e32 v205, v205, v205
	v_max_f32_e32 v205, v205, v206
	v_mov_b32_e32 v206, v205
	s_nop 1
	v_permlane32_swap_b32_e32 v205, v206
	v_max_f32_e32 v206, v206, v206
	v_max_f32_e32 v205, v205, v205
	v_max_f32_e32 v205, v205, v206
	v_cmp_gt_f32_e32 vcc, v205, v179
	s_cbranch_vccz .Lpf2a_815_1
	v_max_f32_e32 v205, v205, v205
	v_max_f32_e32 v206, v179, v179
	v_max_f32_e32 v205, v206, v205
	v_sub_f32_e32 v179, v179, v205
	v_exp_f32_e32 v206, v179
	v_mov_b32_e32 v179, v205
	v_mul_f32_e32 v187, v187, v206
	v_pk_mul_f32 v[20:21], v[20:21], v[206:207] op_sel_hi:[1,0]
	v_pk_mul_f32 v[18:19], v[18:19], v[206:207] op_sel_hi:[1,0]
	v_pk_mul_f32 v[16:17], v[16:17], v[206:207] op_sel_hi:[1,0]
	v_pk_mul_f32 v[14:15], v[14:15], v[206:207] op_sel_hi:[1,0]
	v_pk_mul_f32 v[12:13], v[12:13], v[206:207] op_sel_hi:[1,0]
	v_pk_mul_f32 v[10:11], v[10:11], v[206:207] op_sel_hi:[1,0]
	v_pk_mul_f32 v[8:9], v[8:9], v[206:207] op_sel_hi:[1,0]
	v_pk_mul_f32 v[6:7], v[6:7], v[206:207] op_sel_hi:[1,0]
.Lpf2a_815_1:
	v_add_f32_e32 v138, 0, v138
	v_add_f32_e32 v138, v139, v138
	v_add_f32_e32 v138, v140, v138
	v_add_f32_e32 v138, v141, v138
	v_add_f32_e32 v134, v134, v138
	v_add_f32_e32 v2, 0, v2
	v_add_f32_e32 v134, v135, v134
	v_add_f32_e32 v2, v5, v2
	v_add_f32_e32 v134, v136, v134
	v_add_f32_e32 v2, v191, v2
	v_add_f32_e32 v134, v137, v134
	v_add_f32_e32 v2, v192, v2
	v_add_f32_e32 v188, v188, v134
	v_add_f32_e32 v134, 0, v197
	v_add_f32_e32 v2, v193, v2
	v_add_f32_e32 v134, v198, v134
	v_add_f32_e32 v2, v194, v2
	v_add_f32_e32 v134, v199, v134
	v_add_f32_e32 v2, v195, v2
	v_add_f32_e32 v134, v200, v134
	v_add_f32_e32 v2, v196, v2
	v_add_f32_e32 v134, v201, v134
	v_add_f32_e32 v4, v4, v2
	v_sub_f32_e32 v2, v90, v179
	v_sub_f32_e32 v5, v91, v179
	v_add_f32_e32 v134, v202, v134
	v_exp_f32_e32 v2, v2
	v_exp_f32_e32 v5, v5
	v_sub_f32_e32 v94, v94, v179
	v_add_f32_e32 v134, v203, v134
	v_sub_f32_e32 v90, v92, v179
	v_exp_f32_e32 v92, v94
	v_sub_f32_e32 v94, v95, v179
	v_add_f32_e32 v134, v204, v134
	v_exp_f32_e32 v90, v90
	v_sub_f32_e32 v91, v93, v179
	v_exp_f32_e32 v93, v94
	v_sub_f32_e32 v94, v96, v179
	v_add_f32_e32 v189, v189, v134
	v_exp_f32_e32 v91, v91
	v_exp_f32_e32 v134, v94
	v_sub_f32_e32 v94, v97, v179
	v_exp_f32_e32 v135, v94
	v_cvt_pk_bf16_f32 v94, v2, v5
	v_add_f32_e32 v2, 0, v2
	v_add_f32_e32 v2, v5, v2
	v_add_f32_e32 v2, v90, v2
	v_add_f32_e32 v2, v91, v2
	v_cvt_pk_bf16_f32 v95, v90, v91
	v_cvt_pk_bf16_f32 v96, v92, v93
	v_cvt_pk_bf16_f32 v97, v134, v135
	v_add_f32_e32 v2, v92, v2
	v_add_f32_e32 v2, v93, v2
	v_mfma_f32_16x16x32_bf16 v[18:21], v[106:109], v[94:97], v[18:21]
	v_add_f32_e32 v2, v134, v2
	v_add_f32_e32 v2, v135, v2
	v_add_f32_e32 v187, v187, v2
	v_mfma_f32_16x16x32_bf16 v[14:17], v[110:113], v[94:97], v[14:17]
	v_mfma_f32_16x16x32_bf16 v[10:13], v[118:121], v[94:97], v[10:13]
	v_mfma_f32_16x16x32_bf16 v[6:9], v[122:125], v[94:97], v[6:9]

.Lpf2a_body_2:
	s_add_i32 s8, s7, 1
	s_cmp_gt_u32 s8, 8
	s_cbranch_scc1 .Lpf2a_nopf_2
	s_add_i32 s8, s8, s6
	v_med3_i32 v5, s8, 0, v184
	v_lshl_or_b32 v2, v5, 11, v160
	v_lshl_add_u64 v[94:95], v[172:173], 0, v[2:3]
	v_lshlrev_b32_e32 v2, 12, v5
	v_lshl_add_u64 v[122:123], v[174:175], 0, v[2:3]
	global_load_dwordx4 v[90:93], v[94:95], off
	s_nop 0
	global_load_dwordx4 v[94:97], v[94:95], off offset:1024
	s_nop 0
	global_load_dwordx4 v[106:109], v[122:123], off
	global_load_dwordx4 v[110:113], v[122:123], off offset:1024
	global_load_dwordx4 v[118:121], v[122:123], off offset:2048
	s_nop 0
	global_load_dwordx4 v[122:125], v[122:123], off offset:3072
.Lpf2a_nopf_2:
	s_add_i32 s8, s6, s7
	s_add_i32 s8, s8, -1
	s_cmpk_gt_u32 s8, 0xff
	s_cbranch_scc1 .Lpf2a_816_2
	ds_read2_b32 v[134:135], v190 offset1:1
	ds_read2_b32 v[136:137], v190 offset0:2 offset1:3
	ds_read2_b32 v[192:193], v190 offset0:16 offset1:17
	ds_read2_b32 v[194:195], v190 offset0:18 offset1:19
	s_waitcnt vmcnt(17) lgkmcnt(2)
	v_mfma_f32_16x16x32_fp8_fp8 v[134:137], v[214:215], v[70:71], v[134:137]
	v_mfma_f32_16x16x32_fp8_fp8 v[138:141], v[216:217], v[72:73], v[134:137]
	s_waitcnt vmcnt(16) lgkmcnt(0)
	v_mfma_f32_16x16x32_fp8_fp8 v[134:137], v[218:219], v[70:71], v[192:195]
	v_mfma_f32_16x16x32_fp8_fp8 v[134:137], v[220:221], v[72:73], v[134:137]
	s_nop 4
	v_max_f32_e32 v2, v139, v139
	v_max_f32_e32 v5, v138, v138
	v_max_f32_e32 v2, v5, v2
	v_max_f32_e32 v5, v141, v141
	v_max_f32_e32 v191, v140, v140
	v_max_f32_e32 v5, v191, v5
	v_max_f32_e32 v191, v137, v137
	v_max_f32_e32 v192, v136, v136
	v_max_f32_e32 v191, v192, v191
	v_max3_f32 v191, v134, v135, v191
	v_max3_f32 v2, v2, v5, v191
	v_mov_b32_e32 v5, v2
	s_nop 1
	v_permlane16_swap_b32_e32 v2, v5
	v_max_f32_e32 v5, v5, v5
	v_max_f32_e32 v2, v2, v2
	v_max_f32_e32 v2, v2, v5
	v_mov_b32_e32 v5, v2
	s_nop 1
	v_permlane32_swap_b32_e32 v2, v5
	v_max_f32_e32 v5, v5, v5
	v_max_f32_e32 v2, v2, v2
	v_max_f32_e32 v2, v2, v5
	v_cmp_gt_f32_e32 vcc, v2, v176
	s_cbranch_vccz .Lpf2a_809_2
	v_max_f32_e32 v2, v2, v2
	v_max_f32_e32 v5, v176, v176
	v_max_f32_e32 v5, v5, v2
	v_sub_f32_e32 v2, v176, v5
	v_exp_f32_e32 v2, v2
	v_mov_b32_e32 v176, v5
	v_mul_f32_e32 v4, v4, v2
	v_pk_mul_f32 v[68:69], v[68:69], v[2:3] op_sel_hi:[1,0]
	v_pk_mul_f32 v[66:67], v[66:67], v[2:3] op_sel_hi:[1,0]
	v_pk_mul_f32 v[64:65], v[64:65], v[2:3] op_sel_hi:[1,0]
	v_pk_mul_f32 v[62:63], v[62:63], v[2:3] op_sel_hi:[1,0]
	v_pk_mul_f32 v[60:61], v[60:61], v[2:3] op_sel_hi:[1,0]
	v_pk_mul_f32 v[58:59], v[58:59], v[2:3] op_sel_hi:[1,0]
	v_pk_mul_f32 v[56:57], v[56:57], v[2:3] op_sel_hi:[1,0]
	v_pk_mul_f32 v[54:55], v[54:55], v[2:3] op_sel_hi:[1,0]
.Lpf2a_809_2:
	v_sub_f32_e32 v134, v134, v176
	v_exp_f32_e32 v193, v134
	v_sub_f32_e32 v134, v135, v176
	v_sub_f32_e32 v2, v138, v176
	v_sub_f32_e32 v138, v140, v176
	v_exp_f32_e32 v194, v134
	v_sub_f32_e32 v134, v136, v176
	v_sub_f32_e32 v5, v139, v176
	v_exp_f32_e32 v191, v138
	v_sub_f32_e32 v138, v141, v176
	v_exp_f32_e32 v195, v134
	v_sub_f32_e32 v134, v137, v176
	v_exp_f32_e32 v2, v2
	v_exp_f32_e32 v5, v5
	v_exp_f32_e32 v192, v138
	v_exp_f32_e32 v196, v134
	v_cvt_pk_bf16_f32 v136, v193, v194
	v_cvt_pk_bf16_f32 v134, v2, v5
	v_cvt_pk_bf16_f32 v135, v191, v192
	v_cvt_pk_bf16_f32 v137, v195, v196
	s_waitcnt vmcnt(15)
	s_nop 0
	v_mfma_f32_16x16x32_bf16 v[66:69], v[222:225], v[134:137], v[66:69]
	s_waitcnt vmcnt(14)
	v_mfma_f32_16x16x32_bf16 v[62:65], v[226:229], v[134:137], v[62:65]
	s_waitcnt vmcnt(13)
	v_mfma_f32_16x16x32_bf16 v[58:61], v[230:233], v[134:137], v[58:61]
	s_waitcnt vmcnt(12)
	v_mfma_f32_16x16x32_bf16 v[54:57], v[234:237], v[134:137], v[54:57]
	v_add_u32_e32 v134, 0x504, v190
	v_add_u32_e32 v136, 0x50c, v190
	ds_read2_b32 v[134:135], v134 offset1:1
	ds_read2_b32 v[136:137], v136 offset1:1
	v_add_u32_e32 v138, 0x544, v190
	ds_read2_b32 v[198:199], v138 offset1:1
	v_add_u32_e32 v138, 0x54c, v190
	ds_read2_b32 v[200:201], v138 offset1:1
	s_waitcnt lgkmcnt(2)
	v_mfma_f32_16x16x32_fp8_fp8 v[134:137], v[214:215], v[74:75], v[134:137]
	v_mfma_f32_16x16x32_fp8_fp8 v[138:141], v[216:217], v[76:77], v[134:137]
	s_waitcnt lgkmcnt(0)
	v_mfma_f32_16x16x32_fp8_fp8 v[134:137], v[218:219], v[74:75], v[198:201]
	v_mfma_f32_16x16x32_fp8_fp8 v[134:137], v[220:221], v[76:77], v[134:137]
	s_nop 4
	v_max_f32_e32 v197, v139, v139
	v_max_f32_e32 v198, v138, v138
	v_max_f32_e32 v197, v198, v197
	v_max_f32_e32 v198, v141, v141
	v_max_f32_e32 v199, v140, v140
	v_max_f32_e32 v198, v199, v198
	v_max_f32_e32 v199, v137, v137
	v_max_f32_e32 v200, v136, v136
	v_max_f32_e32 v199, v200, v199
	v_max3_f32 v199, v134, v135, v199
	v_max3_f32 v197, v197, v198, v199
	v_mov_b32_e32 v198, v197
	s_nop 1
	v_permlane16_swap_b32_e32 v197, v198
	v_max_f32_e32 v198, v198, v198
	v_max_f32_e32 v197, v197, v197
	v_max_f32_e32 v197, v197, v198
	v_mov_b32_e32 v198, v197
	s_nop 1
	v_permlane32_swap_b32_e32 v197, v198
	v_max_f32_e32 v198, v198, v198
	v_max_f32_e32 v197, v197, v197
	v_max_f32_e32 v197, v197, v198
	v_cmp_gt_f32_e32 vcc, v197, v177
	s_cbranch_vccz .Lpf2a_811_2
	v_max_f32_e32 v197, v197, v197
	v_max_f32_e32 v198, v177, v177
	v_max_f32_e32 v197, v198, v197
	v_sub_f32_e32 v177, v177, v197
	v_exp_f32_e32 v198, v177
	v_mov_b32_e32 v177, v197
	v_mul_f32_e32 v189, v189, v198
	v_pk_mul_f32 v[52:53], v[52:53], v[198:199] op_sel_hi:[1,0]
	v_pk_mul_f32 v[50:51], v[50:51], v[198:199] op_sel_hi:[1,0]
	v_pk_mul_f32 v[48:49], v[48:49], v[198:199] op_sel_hi:[1,0]
	v_pk_mul_f32 v[46:47], v[46:47], v[198:199] op_sel_hi:[1,0]
	v_pk_mul_f32 v[44:45], v[44:45], v[198:199] op_sel_hi:[1,0]
	v_pk_mul_f32 v[42:43], v[42:43], v[198:199] op_sel_hi:[1,0]
	v_pk_mul_f32 v[40:41], v[40:41], v[198:199] op_sel_hi:[1,0]
	v_pk_mul_f32 v[38:39], v[38:39], v[198:199] op_sel_hi:[1,0]
.Lpf2a_811_2:
	v_sub_f32_e32 v138, v138, v177
	v_sub_f32_e32 v134, v134, v177
	v_exp_f32_e32 v197, v138
	v_sub_f32_e32 v138, v139, v177
	v_exp_f32_e32 v201, v134
	v_sub_f32_e32 v134, v135, v177
	v_exp_f32_e32 v198, v138
	v_sub_f32_e32 v138, v140, v177
	v_exp_f32_e32 v202, v134
	v_sub_f32_e32 v134, v136, v177
	v_exp_f32_e32 v199, v138
	v_sub_f32_e32 v138, v141, v177
	v_exp_f32_e32 v203, v134
	v_sub_f32_e32 v134, v137, v177
	v_exp_f32_e32 v200, v138
	v_exp_f32_e32 v204, v134
	v_cvt_pk_bf16_f32 v134, v197, v198
	v_cvt_pk_bf16_f32 v136, v201, v202
	v_cvt_pk_bf16_f32 v135, v199, v200
	v_cvt_pk_bf16_f32 v137, v203, v204
	s_nop 1
	v_mfma_f32_16x16x32_bf16 v[50:53], v[222:225], v[134:137], v[50:53]
	v_mfma_f32_16x16x32_bf16 v[46:49], v[226:229], v[134:137], v[46:49]
	v_mfma_f32_16x16x32_bf16 v[42:45], v[230:233], v[134:137], v[42:45]
	v_mfma_f32_16x16x32_bf16 v[38:41], v[234:237], v[134:137], v[38:41]
	v_add_u32_e32 v134, 0xa08, v190
	v_add_u32_e32 v136, 0xa10, v190
	ds_read2_b32 v[134:135], v134 offset1:1
	ds_read2_b32 v[136:137], v136 offset1:1
	v_add_u32_e32 v138, 0xa48, v190
	ds_read2_b32 v[206:207], v138 offset1:1
	v_add_u32_e32 v138, 0xa50, v190
	ds_read2_b32 v[208:209], v138 offset1:1
	s_waitcnt lgkmcnt(2)
	v_mfma_f32_16x16x32_fp8_fp8 v[134:137], v[214:215], v[78:79], v[134:137]
	v_mfma_f32_16x16x32_fp8_fp8 v[138:141], v[216:217], v[80:81], v[134:137]
	s_waitcnt lgkmcnt(0)
	v_mfma_f32_16x16x32_fp8_fp8 v[134:137], v[218:219], v[78:79], v[206:209]
	v_mfma_f32_16x16x32_fp8_fp8 v[134:137], v[220:221], v[80:81], v[134:137]
	s_nop 4
	v_max_f32_e32 v205, v139, v139
	v_max_f32_e32 v206, v138, v138
	v_max_f32_e32 v205, v206, v205
	v_max_f32_e32 v206, v141, v141
	v_max_f32_e32 v207, v140, v140
	v_max_f32_e32 v206, v207, v206
	v_max_f32_e32 v207, v137, v137
	v_max_f32_e32 v208, v136, v136
	v_max_f32_e32 v207, v208, v207
	v_max3_f32 v207, v134, v135, v207
	v_max3_f32 v205, v205, v206, v207
	v_mov_b32_e32 v206, v205
	s_nop 1
	v_permlane16_swap_b32_e32 v205, v206
	v_max_f32_e32 v206, v206, v206
	v_max_f32_e32 v205, v205, v205
	v_max_f32_e32 v205, v205, v206
	v_mov_b32_e32 v206, v205
	s_nop 1
	v_permlane32_swap_b32_e32 v205, v206
	v_max_f32_e32 v206, v206, v206
	v_max_f32_e32 v205, v205, v205
	v_max_f32_e32 v205, v205, v206
	v_cmp_gt_f32_e32 vcc, v205, v178
	s_cbranch_vccz .Lpf2a_813_2
	v_max_f32_e32 v205, v205, v205
	v_max_f32_e32 v206, v178, v178
	v_max_f32_e32 v205, v206, v205
	v_sub_f32_e32 v178, v178, v205
	v_exp_f32_e32 v178, v178
	s_nop 0
	v_mul_f32_e32 v188, v188, v178
	v_pk_mul_f32 v[36:37], v[36:37], v[178:179] op_sel_hi:[1,0]
	v_pk_mul_f32 v[34:35], v[34:35], v[178:179] op_sel_hi:[1,0]
	v_pk_mul_f32 v[32:33], v[32:33], v[178:179] op_sel_hi:[1,0]
	v_pk_mul_f32 v[30:31], v[30:31], v[178:179] op_sel_hi:[1,0]
	v_pk_mul_f32 v[28:29], v[28:29], v[178:179] op_sel_hi:[1,0]
	v_pk_mul_f32 v[26:27], v[26:27], v[178:179] op_sel_hi:[1,0]
	v_pk_mul_f32 v[24:25], v[24:25], v[178:179] op_sel_hi:[1,0]
	v_pk_mul_f32 v[22:23], v[22:23], v[178:179] op_sel_hi:[1,0]
	v_mov_b32_e32 v178, v205
.Lpf2a_813_2:
	v_sub_f32_e32 v138, v138, v178
	v_sub_f32_e32 v139, v139, v178
	v_sub_f32_e32 v140, v140, v178
	v_sub_f32_e32 v141, v141, v178
	v_sub_f32_e32 v134, v134, v178
	v_sub_f32_e32 v135, v135, v178
	v_sub_f32_e32 v136, v136, v178
	v_sub_f32_e32 v137, v137, v178
	v_exp_f32_e32 v138, v138
	v_exp_f32_e32 v139, v139
	v_exp_f32_e32 v140, v140
	v_exp_f32_e32 v141, v141
	v_exp_f32_e32 v134, v134
	v_exp_f32_e32 v135, v135
	v_exp_f32_e32 v136, v136
	v_exp_f32_e32 v137, v137
	v_cvt_pk_bf16_f32 v206, v138, v139
	v_cvt_pk_bf16_f32 v207, v140, v141
	v_cvt_pk_bf16_f32 v208, v134, v135
	v_cvt_pk_bf16_f32 v209, v136, v137
	s_nop 1
	v_mfma_f32_16x16x32_bf16 v[34:37], v[222:225], v[206:209], v[34:37]
	v_mfma_f32_16x16x32_bf16 v[30:33], v[226:229], v[206:209], v[30:33]
	v_mfma_f32_16x16x32_bf16 v[26:29], v[230:233], v[206:209], v[26:29]
	v_mfma_f32_16x16x32_bf16 v[22:25], v[234:237], v[206:209], v[22:25]
	v_add_u32_e32 v205, 0xf0c, v190
	v_add_u32_e32 v208, 0xf14, v190
	ds_read2_b32 v[206:207], v205 offset1:1
	ds_read2_b32 v[208:209], v208 offset1:1
	v_add_u32_e32 v205, 0xf4c, v190
	v_add_u32_e32 v212, 0xf54, v190
	ds_read2_b32 v[210:211], v205 offset1:1
	ds_read2_b32 v[212:213], v212 offset1:1
	s_waitcnt lgkmcnt(2)
	v_mfma_f32_16x16x32_fp8_fp8 v[206:209], v[214:215], v[82:83], v[206:209]
	s_waitcnt lgkmcnt(0)
	v_mfma_f32_16x16x32_fp8_fp8 v[210:213], v[218:219], v[82:83], v[210:213]
	v_mfma_f32_16x16x32_fp8_fp8 v[214:217], v[216:217], v[84:85], v[206:209]
	v_mfma_f32_16x16x32_fp8_fp8 v[218:221], v[220:221], v[84:85], v[210:213]
	s_nop 6
	v_max_f32_e32 v205, v215, v215
	v_max_f32_e32 v206, v214, v214
	v_max_f32_e32 v207, v217, v217
	v_max_f32_e32 v205, v206, v205
	v_max_f32_e32 v206, v216, v216
	v_max_f32_e32 v206, v206, v207
	v_max_f32_e32 v207, v221, v221
	v_max_f32_e32 v208, v220, v220
	v_max_f32_e32 v207, v208, v207
	v_max3_f32 v207, v218, v219, v207
	v_max3_f32 v205, v205, v206, v207
	v_mov_b32_e32 v206, v205
	s_nop 1
	v_permlane16_swap_b32_e32 v205, v206
	v_max_f32_e32 v206, v206, v206
	v_max_f32_e32 v205, v205, v205
	v_max_f32_e32 v205, v205, v206
	v_mov_b32_e32 v206, v205
	s_nop 1
	v_permlane32_swap_b32_e32 v205, v206
	v_max_f32_e32 v206, v206, v206
	v_max_f32_e32 v205, v205, v205
	v_max_f32_e32 v205, v205, v206
	v_cmp_gt_f32_e32 vcc, v205, v179
	s_cbranch_vccz .Lpf2a_815_2
	v_max_f32_e32 v205, v205, v205
	v_max_f32_e32 v206, v179, v179
	v_max_f32_e32 v205, v206, v205
	v_sub_f32_e32 v179, v179, v205
	v_exp_f32_e32 v206, v179
	v_mov_b32_e32 v179, v205
	v_mul_f32_e32 v187, v187, v206
	v_pk_mul_f32 v[20:21], v[20:21], v[206:207] op_sel_hi:[1,0]
	v_pk_mul_f32 v[18:19], v[18:19], v[206:207] op_sel_hi:[1,0]
	v_pk_mul_f32 v[16:17], v[16:17], v[206:207] op_sel_hi:[1,0]
	v_pk_mul_f32 v[14:15], v[14:15], v[206:207] op_sel_hi:[1,0]
	v_pk_mul_f32 v[12:13], v[12:13], v[206:207] op_sel_hi:[1,0]
	v_pk_mul_f32 v[10:11], v[10:11], v[206:207] op_sel_hi:[1,0]
	v_pk_mul_f32 v[8:9], v[8:9], v[206:207] op_sel_hi:[1,0]
	v_pk_mul_f32 v[6:7], v[6:7], v[206:207] op_sel_hi:[1,0]
.Lpf2a_815_2:
	v_add_f32_e32 v138, 0, v138
	v_add_f32_e32 v138, v139, v138
	v_add_f32_e32 v138, v140, v138
	v_add_f32_e32 v138, v141, v138
	v_add_f32_e32 v134, v134, v138
	v_add_f32_e32 v2, 0, v2
	v_add_f32_e32 v134, v135, v134
	v_add_f32_e32 v2, v5, v2
	v_add_f32_e32 v134, v136, v134
	v_add_f32_e32 v2, v191, v2
	v_add_f32_e32 v134, v137, v134
	v_add_f32_e32 v2, v192, v2
	v_add_f32_e32 v188, v188, v134
	v_add_f32_e32 v134, 0, v197
	v_add_f32_e32 v2, v193, v2
	v_add_f32_e32 v134, v198, v134
	v_add_f32_e32 v2, v194, v2
	v_add_f32_e32 v134, v199, v134
	v_add_f32_e32 v2, v195, v2
	v_add_f32_e32 v134, v200, v134
	v_add_f32_e32 v2, v196, v2
	v_add_f32_e32 v134, v201, v134
	v_add_f32_e32 v4, v4, v2
	v_sub_f32_e32 v2, v214, v179
	v_sub_f32_e32 v5, v215, v179
	v_add_f32_e32 v134, v202, v134
	v_exp_f32_e32 v2, v2
	v_exp_f32_e32 v5, v5
	v_sub_f32_e32 v218, v218, v179
	v_add_f32_e32 v134, v203, v134
	v_sub_f32_e32 v214, v216, v179
	v_exp_f32_e32 v216, v218
	v_sub_f32_e32 v218, v219, v179
	v_add_f32_e32 v134, v204, v134
	v_exp_f32_e32 v214, v214
	v_sub_f32_e32 v215, v217, v179
	v_exp_f32_e32 v217, v218
	v_sub_f32_e32 v218, v220, v179
	v_add_f32_e32 v189, v189, v134
	v_exp_f32_e32 v215, v215
	v_exp_f32_e32 v134, v218
	v_sub_f32_e32 v218, v221, v179
	v_exp_f32_e32 v135, v218
	v_cvt_pk_bf16_f32 v218, v2, v5
	v_add_f32_e32 v2, 0, v2
	v_add_f32_e32 v2, v5, v2
	v_add_f32_e32 v2, v214, v2
	v_add_f32_e32 v2, v215, v2
	v_cvt_pk_bf16_f32 v219, v214, v215
	v_cvt_pk_bf16_f32 v220, v216, v217
	v_cvt_pk_bf16_f32 v221, v134, v135
	v_add_f32_e32 v2, v216, v2
	v_add_f32_e32 v2, v217, v2
	v_mfma_f32_16x16x32_bf16 v[18:21], v[222:225], v[218:221], v[18:21]
	v_add_f32_e32 v2, v134, v2
	v_add_f32_e32 v2, v135, v2
	v_add_f32_e32 v187, v187, v2
	v_mfma_f32_16x16x32_bf16 v[14:17], v[226:229], v[218:221], v[14:17]
	v_mfma_f32_16x16x32_bf16 v[10:13], v[230:233], v[218:221], v[10:13]
	v_mfma_f32_16x16x32_bf16 v[6:9], v[234:237], v[218:221], v[6:9]
